# speedup vs baseline: 1.0331x; 1.0119x over previous
.Lq_noprio:
	s_nop 0
	s_waitcnt vmcnt(12)
	v_cvt_pk_f16_f32 v164, v36, v40
	v_cvt_pk_f16_f32 v180, v68, v72
	v_pk_add_f16 v164, v164, -0.5 op_sel_hi:[1,0]
	v_pk_add_f16 v180, v180, -0.5 op_sel_hi:[1,0]
	v_pk_mul_f16 v196, v180, v180
	v_pk_mul_f16 v212, v164, v180
	v_pk_fma_f16 v196, v164, v164, v196
	v_cvt_pk_f16_f32 v168, v37, v41
	v_cvt_pk_f16_f32 v184, v69, v73
	v_pk_add_f16 v168, v168, -0.5 op_sel_hi:[1,0]
	v_pk_add_f16 v184, v184, -0.5 op_sel_hi:[1,0]
	v_pk_mul_f16 v200, v184, v184
	v_pk_mul_f16 v216, v168, v184
	v_pk_fma_f16 v200, v168, v168, v200
	v_cvt_pk_f16_f32 v172, v38, v42
	v_cvt_pk_f16_f32 v188, v70, v74
	v_pk_add_f16 v172, v172, -0.5 op_sel_hi:[1,0]
	v_pk_add_f16 v188, v188, -0.5 op_sel_hi:[1,0]
	v_pk_mul_f16 v204, v188, v188
	v_pk_mul_f16 v220, v172, v188
	v_pk_fma_f16 v204, v172, v172, v204
	v_cvt_pk_f16_f32 v176, v39, v43
	v_cvt_pk_f16_f32 v192, v71, v75
	v_pk_add_f16 v176, v176, -0.5 op_sel_hi:[1,0]
	v_pk_add_f16 v192, v192, -0.5 op_sel_hi:[1,0]
	v_pk_mul_f16 v208, v192, v192
	v_pk_mul_f16 v224, v176, v192
	v_pk_fma_f16 v208, v176, v176, v208
	s_waitcnt vmcnt(8)
	v_cvt_pk_f16_f32 v165, v44, v48
	v_cvt_pk_f16_f32 v181, v76, v80
	v_pk_add_f16 v165, v165, -0.5 op_sel_hi:[1,0]
	v_pk_add_f16 v181, v181, -0.5 op_sel_hi:[1,0]
	v_pk_mul_f16 v197, v181, v181
	v_pk_mul_f16 v213, v165, v181
	v_pk_fma_f16 v197, v165, v165, v197
	v_cvt_pk_f16_f32 v169, v45, v49
	v_cvt_pk_f16_f32 v185, v77, v81
	v_pk_add_f16 v169, v169, -0.5 op_sel_hi:[1,0]
	v_pk_add_f16 v185, v185, -0.5 op_sel_hi:[1,0]
	v_pk_mul_f16 v201, v185, v185
	v_pk_mul_f16 v217, v169, v185
	v_pk_fma_f16 v201, v169, v169, v201
	v_cvt_pk_f16_f32 v173, v46, v50
	v_cvt_pk_f16_f32 v189, v78, v82
	v_pk_add_f16 v173, v173, -0.5 op_sel_hi:[1,0]
	v_pk_add_f16 v189, v189, -0.5 op_sel_hi:[1,0]
	v_pk_mul_f16 v205, v189, v189
	v_pk_mul_f16 v221, v173, v189
	v_pk_fma_f16 v205, v173, v173, v205
	v_cvt_pk_f16_f32 v177, v47, v51
	v_cvt_pk_f16_f32 v193, v79, v83
	v_pk_add_f16 v177, v177, -0.5 op_sel_hi:[1,0]
	v_pk_add_f16 v193, v193, -0.5 op_sel_hi:[1,0]
	v_pk_mul_f16 v209, v193, v193
	v_pk_mul_f16 v225, v177, v193
	v_pk_fma_f16 v209, v177, v177, v209
	s_waitcnt vmcnt(4)
	v_cvt_pk_f16_f32 v166, v52, v56
	v_cvt_pk_f16_f32 v182, v84, v88
	v_pk_add_f16 v166, v166, -0.5 op_sel_hi:[1,0]
	v_pk_add_f16 v182, v182, -0.5 op_sel_hi:[1,0]
	v_pk_mul_f16 v198, v182, v182
	v_pk_mul_f16 v214, v166, v182
	v_pk_fma_f16 v198, v166, v166, v198
	v_cvt_pk_f16_f32 v170, v53, v57
	v_cvt_pk_f16_f32 v186, v85, v89
	v_pk_add_f16 v170, v170, -0.5 op_sel_hi:[1,0]
	v_pk_add_f16 v186, v186, -0.5 op_sel_hi:[1,0]
	v_pk_mul_f16 v202, v186, v186
	v_pk_mul_f16 v218, v170, v186
	v_pk_fma_f16 v202, v170, v170, v202
	v_cvt_pk_f16_f32 v174, v54, v58
	v_cvt_pk_f16_f32 v190, v86, v90
	v_pk_add_f16 v174, v174, -0.5 op_sel_hi:[1,0]
	v_pk_add_f16 v190, v190, -0.5 op_sel_hi:[1,0]
	v_pk_mul_f16 v206, v190, v190
	v_pk_mul_f16 v222, v174, v190
	v_pk_fma_f16 v206, v174, v174, v206
	v_cvt_pk_f16_f32 v178, v55, v59
	v_cvt_pk_f16_f32 v194, v87, v91
	v_pk_add_f16 v178, v178, -0.5 op_sel_hi:[1,0]
	v_pk_add_f16 v194, v194, -0.5 op_sel_hi:[1,0]
	v_pk_mul_f16 v210, v194, v194
	v_pk_mul_f16 v226, v178, v194
	v_pk_fma_f16 v210, v178, v178, v210
	s_waitcnt vmcnt(0)
	v_cvt_pk_f16_f32 v167, v60, v64
	v_cvt_pk_f16_f32 v183, v92, v96
	v_pk_add_f16 v167, v167, -0.5 op_sel_hi:[1,0]
	v_pk_add_f16 v183, v183, -0.5 op_sel_hi:[1,0]
	v_pk_mul_f16 v199, v183, v183
	v_pk_mul_f16 v215, v167, v183
	v_pk_fma_f16 v199, v167, v167, v199
	v_cvt_pk_f16_f32 v171, v61, v65
	v_cvt_pk_f16_f32 v187, v93, v97
	v_pk_add_f16 v171, v171, -0.5 op_sel_hi:[1,0]
	v_pk_add_f16 v187, v187, -0.5 op_sel_hi:[1,0]
	v_pk_mul_f16 v203, v187, v187
	v_pk_mul_f16 v219, v171, v187
	v_pk_fma_f16 v203, v171, v171, v203
	v_cvt_pk_f16_f32 v175, v62, v66
	v_cvt_pk_f16_f32 v191, v94, v98
	v_pk_add_f16 v175, v175, -0.5 op_sel_hi:[1,0]
	v_pk_add_f16 v191, v191, -0.5 op_sel_hi:[1,0]
	v_pk_mul_f16 v207, v191, v191
	v_pk_mul_f16 v223, v175, v191
	v_pk_fma_f16 v207, v175, v175, v207
	v_cvt_pk_f16_f32 v179, v63, v67
	v_cvt_pk_f16_f32 v195, v95, v99
	v_pk_add_f16 v179, v179, -0.5 op_sel_hi:[1,0]
	v_pk_add_f16 v195, v195, -0.5 op_sel_hi:[1,0]
	v_pk_mul_f16 v211, v195, v195
	v_pk_mul_f16 v227, v179, v195
	v_pk_fma_f16 v211, v179, v179, v211
	global_load_dwordx4 v[100:103], v240, s[18:19] offset:0 sc1 nt
	global_load_dwordx4 v[104:107], v240, s[18:19] offset:2048 sc1 nt
	global_load_dwordx4 v[132:135], v240, s[20:21] offset:0 sc1 nt
	global_load_dwordx4 v[136:139], v240, s[20:21] offset:2048 sc1 nt
	global_load_dwordx4 v[108:111], v241, s[18:19] offset:0 sc1 nt
	global_load_dwordx4 v[112:115], v241, s[18:19] offset:2048 sc1 nt
	global_load_dwordx4 v[140:143], v241, s[20:21] offset:0 sc1 nt
	global_load_dwordx4 v[144:147], v241, s[20:21] offset:2048 sc1 nt
	global_load_dwordx4 v[116:119], v242, s[18:19] offset:0 sc1 nt
	global_load_dwordx4 v[120:123], v242, s[18:19] offset:2048 sc1 nt
	global_load_dwordx4 v[148:151], v242, s[20:21] offset:0 sc1 nt
	global_load_dwordx4 v[152:155], v242, s[20:21] offset:2048 sc1 nt
	global_load_dwordx4 v[124:127], v243, s[18:19] offset:0 sc1 nt
	global_load_dwordx4 v[128:131], v243, s[18:19] offset:2048 sc1 nt
	global_load_dwordx4 v[156:159], v243, s[20:21] offset:0 sc1 nt
	global_load_dwordx4 v[160:163], v243, s[20:21] offset:2048 sc1 nt
	v_mfma_f32_16x16x32_f16 v[68:71], v[164:167], v[24:27], 0
	v_mfma_f32_16x16x32_f16 v[72:75], v[168:171], v[24:27], 0
	v_mfma_f32_16x16x32_f16 v[76:79], v[172:175], v[24:27], 0
	v_mfma_f32_16x16x32_f16 v[80:83], v[176:179], v[24:27], 0
	v_mfma_f32_16x16x32_f16 v[84:87], v[180:183], v[24:27], 0
	v_mfma_f32_16x16x32_f16 v[88:91], v[184:187], v[24:27], 0
	v_mfma_f32_16x16x32_f16 v[92:95], v[188:191], v[24:27], 0
	v_mfma_f32_16x16x32_f16 v[96:99], v[192:195], v[24:27], 0
	s_nop 1
	v_cvt_pk_f16_f32 v36, v68, v72
	s_nop 0
	v_cvt_pk_f16_f32 v37, v76, v80
	v_cvt_pk_f16_f32 v38, v69, v73
	v_cvt_pk_f16_f32 v39, v77, v81
	v_cvt_pk_f16_f32 v40, v70, v74
	v_cvt_pk_f16_f32 v41, v78, v82
	v_cvt_pk_f16_f32 v42, v71, v75
	v_cvt_pk_f16_f32 v43, v79, v83
	v_mfma_f32_16x16x32_f16 v[68:71], v[196:199], v[24:27], 0
	v_mfma_f32_16x16x32_f16 v[72:75], v[200:203], v[24:27], 0
	v_mfma_f32_16x16x32_f16 v[76:79], v[204:207], v[24:27], 0
	v_mfma_f32_16x16x32_f16 v[80:83], v[208:211], v[24:27], 0
	v_cvt_pk_f16_f32 v44, v84, v88
	v_cvt_pk_f16_f32 v45, v92, v96
	v_cvt_pk_f16_f32 v46, v85, v89
	v_cvt_pk_f16_f32 v47, v93, v97
	v_cvt_pk_f16_f32 v48, v86, v90
	v_cvt_pk_f16_f32 v49, v94, v98
	v_cvt_pk_f16_f32 v50, v87, v91
	v_cvt_pk_f16_f32 v51, v95, v99
	v_mfma_f32_16x16x32_f16 v[84:87], v[212:215], v[24:27], 0
	v_mfma_f32_16x16x32_f16 v[88:91], v[216:219], v[24:27], 0
	v_mfma_f32_16x16x32_f16 v[92:95], v[220:223], v[24:27], 0
	v_mfma_f32_16x16x32_f16 v[96:99], v[224:227], v[24:27], 0
	v_cvt_pk_f16_f32 v52, v68, v72
	v_cvt_pk_f16_f32 v53, v76, v80
	v_cvt_pk_f16_f32 v54, v69, v73
	v_cvt_pk_f16_f32 v55, v77, v81
	v_cvt_pk_f16_f32 v56, v70, v74
	v_cvt_pk_f16_f32 v57, v78, v82
	v_cvt_pk_f16_f32 v58, v71, v75
	v_cvt_pk_f16_f32 v59, v79, v83
	v_cvt_pk_f16_f32 v60, v84, v88
	v_cvt_pk_f16_f32 v61, v92, v96
	v_cvt_pk_f16_f32 v62, v85, v89
	v_cvt_pk_f16_f32 v63, v93, v97
	v_cvt_pk_f16_f32 v64, v86, v90
	v_cvt_pk_f16_f32 v65, v94, v98
	v_cvt_pk_f16_f32 v66, v87, v91
	v_cvt_pk_f16_f32 v67, v95, v99
	s_mov_b64 exec, s[38:39]
	ds_write_b128 v4, v[40:43] offset:0
	ds_write_b128 v4, v[48:51] offset:512
	ds_write_b128 v4, v[56:59] offset:1024
	ds_write_b128 v4, v[64:67] offset:1536
	s_mov_b64 exec, -1
	v_mfma_f32_16x16x32_f16 v[68:71], v[24:27], v[36:39], 0
	v_mfma_f32_16x16x32_f16 v[72:75], v[24:27], v[44:47], 0
	v_mfma_f32_16x16x32_f16 v[76:79], v[24:27], v[52:55], v[0:3]
	v_mfma_f32_16x16x32_f16 v[80:83], v[24:27], v[60:63], 0
	v_mfma_f32_16x16x32_f16 v[84:87], v[28:31], v[36:39], 0
	v_mfma_f32_16x16x32_f16 v[88:91], v[28:31], v[44:47], 0
	v_mfma_f32_16x16x32_f16 v[92:95], v[28:31], v[52:55], v[0:3]
	v_mfma_f32_16x16x32_f16 v[96:99], v[28:31], v[60:63], 0
	v_mfma_f32_16x16x32_f16 v[84:87], v[32:35], v[40:43], v[84:87]
	v_mfma_f32_16x16x32_f16 v[88:91], v[32:35], v[48:51], v[88:91]
	v_mfma_f32_16x16x32_f16 v[92:95], v[32:35], v[56:59], v[92:95]
	v_mfma_f32_16x16x32_f16 v[96:99], v[32:35], v[64:67], v[96:99]
	s_waitcnt lgkmcnt(0)
	ds_write_b32 v6, v6 offset:0
	ds_read_b32 v9, v7 offset:0
	v_mul_f32_e32 v244, v68, v72
	v_mul_f32_e32 v250, v69, v73
	v_mul_f32_e64 v245, -v72, v72
	v_mul_f32_e64 v251, -v73, v73
	v_add_f32_e32 v246, v68, v72
	v_add_f32_e32 v252, v69, v73
	v_fma_f32 v245, -v68, v68, v245
	v_fma_f32 v251, -v69, v69, v251
	v_fma_f32 v247, v10, v246, v11
	v_fma_f32 v253, v10, v252, v11
	v_fma_f32 v246, v13, v80, v14
	v_fma_f32 v252, v13, v81, v14
	v_fma_f32 v248, v12, v76, v245
	v_fma_f32 v254, v12, v77, v251
	v_fma_f32 v249, 2.0, v244, v247
	v_fma_f32 v255, 2.0, v250, v253
	v_sub_f32_e32 v247, v247, v245
	v_sub_f32_e32 v253, v253, v251
	v_fma_f32 v246, -2.0, v244, v246
	v_fma_f32 v252, -2.0, v250, v252
	v_mul_f32_e32 v247, v247, v248
	v_mul_f32_e32 v253, v253, v254
	v_rcp_f32_e32 v247, v247
	v_rcp_f32_e32 v253, v253
	v_mul_f32_e32 v249, v249, v246
	v_mul_f32_e32 v255, v255, v252
	v_fma_f32 v19, v249, v247, v19
	v_fma_f32 v19, v255, v253, v19
	v_mul_f32_e32 v244, v70, v74
	v_mul_f32_e32 v250, v71, v75
	v_mul_f32_e64 v245, -v74, v74
	v_mul_f32_e64 v251, -v75, v75
	v_add_f32_e32 v246, v70, v74
	v_add_f32_e32 v252, v71, v75
	v_fma_f32 v245, -v70, v70, v245
	v_fma_f32 v251, -v71, v71, v251
	v_fma_f32 v247, v10, v246, v11
	v_fma_f32 v253, v10, v252, v11
	v_fma_f32 v246, v13, v82, v14
	v_fma_f32 v252, v13, v83, v14
	v_fma_f32 v248, v12, v78, v245
	v_fma_f32 v254, v12, v79, v251
	v_fma_f32 v249, 2.0, v244, v247
	v_fma_f32 v255, 2.0, v250, v253
	v_sub_f32_e32 v247, v247, v245
	v_sub_f32_e32 v253, v253, v251
	v_fma_f32 v246, -2.0, v244, v246
	v_fma_f32 v252, -2.0, v250, v252
	v_mul_f32_e32 v247, v247, v248
	v_mul_f32_e32 v253, v253, v254
	v_rcp_f32_e32 v247, v247
	v_rcp_f32_e32 v253, v253
	v_mul_f32_e32 v249, v249, v246
	v_mul_f32_e32 v255, v255, v252
	v_fma_f32 v20, v249, v247, v20
	v_fma_f32 v20, v255, v253, v20
	v_mfma_f32_16x16x32_f16 v[68:71], v[24:27], v[40:43], 0
	v_mfma_f32_16x16x32_f16 v[72:75], v[24:27], v[48:51], 0
	v_mfma_f32_16x16x32_f16 v[76:79], v[24:27], v[56:59], v[0:3]
	v_mfma_f32_16x16x32_f16 v[80:83], v[24:27], v[64:67], 0
	s_waitcnt lgkmcnt(0)
	v_cmp_ne_u32_e32 vcc, 0, v9
	s_cbranch_vccnz .Lq_go_0
